# baseline (speedup 1.0000x reference)
.Lmain_noprio:
	s_waitcnt lgkmcnt(0)
	s_and_b32 s13, s13, 0xffff
	v_lshlrev_b32_e32 v105, 9, v112
	v_lshlrev_b32_e32 v2, 6, v112
	v_lshlrev_b32_e32 v3, 4, v1
	s_cmp_lt_u32 s44, s42
	s_mov_b32 s7, 0x20000
	v_bitop3_b32 v113, v2, v105, v3 bitop3:0xde
	s_mov_b32 s6, 0x1e848000
	s_cselect_b64 s[8:9], -1, 0
	v_lshlrev_b32_e32 v102, 2, v1
	v_lshlrev_b32_e32 v14, 4, v104
	v_mov_b32_e32 v15, 0
	v_lshl_add_u64 v[6:7], s[16:17], 0, v[14:15]
	v_add_co_u32_e32 v16, vcc, 0x3000, v6
	v_min_u32_e32 v6, 0x1ff, v104
	s_nop 0
	v_addc_co_u32_e32 v17, vcc, 0, v7, vcc
	v_lshlrev_b32_e32 v7, 2, v6
	global_load_dword v15, v7, s[10:11]
	global_load_dwordx4 v[2:5], v14, s[16:17]
	v_lshlrev_b32_e32 v18, 4, v6
	v_or_b32_e32 v19, 0x6000, v18
	global_load_dwordx4 v[6:9], v[16:17], off
	global_load_dwordx4 v[10:13], v19, s[16:17]
	v_min_u32_e32 v16, 0x17f, v104
	v_lshlrev_b32_e32 v16, 2, v16
	global_load_dword v17, v16, s[18:19]
	s_cmp_ge_u32 s44, s42
	s_cbranch_scc1 .Lmain_nodma
	s_lshl_b32 s2, s44, 13
	s_add_i32 m0, s33, 0x8000
	s_mov_b32 s4, s12
	s_mov_b32 s5, s13
	buffer_load_dwordx4 v113, s[4:7], s2 offen sc0 nt lds
	s_add_i32 m0, s33, 0x8400
	s_or_b32 s3, s2, 0x800
	buffer_load_dwordx4 v113, s[4:7], s3 offen sc0 nt lds
	s_add_i32 m0, s33, 0x8800
	s_or_b32 s3, s2, 0x1000
	buffer_load_dwordx4 v113, s[4:7], s3 offen sc0 nt lds
	s_add_i32 m0, s33, 0x8c00
	s_or_b32 s3, s2, 0x1800
	buffer_load_dwordx4 v113, s[4:7], s3 offen sc0 nt lds
	s_add_i32 m0, s33, 0x9000
	s_or_b32 s3, s2, 0x100
	buffer_load_dwordx4 v113, s[4:7], s3 offen sc0 nt lds
	s_add_i32 m0, s33, 0x9400
	s_or_b32 s3, s2, 0x900
	buffer_load_dwordx4 v113, s[4:7], s3 offen sc0 nt lds
	s_add_i32 m0, s33, 0x9800
	s_or_b32 s3, s2, 0x1100
	buffer_load_dwordx4 v113, s[4:7], s3 offen sc0 nt lds
	s_add_i32 m0, s33, 0x9c00
	s_or_b32 s2, s2, 0x1900
	buffer_load_dwordx4 v113, s[4:7], s2 offen sc0 nt lds
	s_lshl_b32 s2, s44, 6
	s_add_u32 s2, s14, s2
	s_addc_u32 s3, s15, 0
	s_mov_b32 m0, s43
	s_nop 0
	global_load_lds_dword v102, s[2:3]

.LBB1_12:
	s_mov_b32 s0, s44
	s_add_i32 s44, s44, 1
	s_cmp_ge_u32 s44, s42
	s_cselect_b64 s[22:23], -1, 0
	s_cmp_lt_u32 s44, s42
	s_cselect_b32 s2, s44, s0
	s_waitcnt vmcnt(0)
	s_lshl_b32 s0, s2, 4
	s_mov_b32 s1, s17
	s_mov_b32 m0, s43
	ds_read_b128 v[76:79], v119 offset:32768
	ds_read_b128 v[80:83], v119 offset:36864
	ds_read_b128 v[84:87], v120 offset:32768
	ds_read_b128 v[88:91], v120 offset:36864
	ds_read_b128 v[92:95], v121
	ds_read_b128 v[96:99], v121 offset:4096
	ds_read_b128 v[128:131], v122
	ds_read_b128 v[132:135], v122 offset:4096
	ds_read_b128 v[72:75], v123
	s_waitcnt lgkmcnt(0)
	v_lshl_add_u64 v[70:71], s[0:1], 2, v[2:3]
	global_load_lds_dword v[70:71], off
	ds_read_b128 v[156:159], v115
	ds_read_b128 v[160:163], v115 offset:1024
	ds_read_b128 v[164:167], v115 offset:2048
	v_cvt_pk_bf16_f32 v136, v76, v77
	v_cvt_pk_bf16_f32 v137, v78, v79
	v_cvt_pk_bf16_f32 v138, v84, v85
	v_cvt_pk_bf16_f32 v139, v86, v87
	v_cvt_pk_bf16_f32 v140, v92, v93
	v_cvt_pk_bf16_f32 v141, v94, v95
	v_cvt_pk_bf16_f32 v142, v128, v129
	v_cvt_pk_bf16_f32 v143, v130, v131
	v_cvt_pk_bf16_f32 v144, v80, v81
	v_cvt_pk_bf16_f32 v145, v82, v83
	v_cvt_pk_bf16_f32 v146, v88, v89
	v_cvt_pk_bf16_f32 v147, v90, v91
	v_cvt_pk_bf16_f32 v128, v96, v97
	v_cvt_pk_bf16_f32 v129, v98, v99
	v_cvt_pk_bf16_f32 v130, v132, v133
	v_cvt_pk_bf16_f32 v131, v134, v135
	s_lshl_b32 s0, s2, 13
	s_cmp_lt_u32 s44, s42
	s_cselect_b32 s0, s0, 0x1e848000
	s_mov_b32 s61, s0
	s_add_i32 s63, s44, 1
	s_cmp_eq_u32 s63, s42
	s_cselect_b32 s63, 1, 0
	ds_read_b128 v[132:135], v115 offset:3072
	s_waitcnt lgkmcnt(3)
	v_mfma_f32_16x16x32_bf16 v[148:151], v[136:139], v[156:159], v[36:39]
	ds_read_b128 v[156:159], v115 offset:4096
	s_waitcnt lgkmcnt(3)
	v_mfma_f32_16x16x32_bf16 v[152:155], v[136:139], v[160:163], v[40:43]
	ds_read_b128 v[160:163], v115 offset:5120
	s_waitcnt lgkmcnt(3)
	v_mfma_f32_16x16x32_bf16 v[96:99], v[136:139], v[164:167], v[44:47]
	ds_read_b128 v[164:167], v115 offset:6144
	s_waitcnt lgkmcnt(3)
	v_mfma_f32_16x16x32_bf16 v[92:95], v[136:139], v[132:135], v[48:51]
	ds_read_b128 v[132:135], v115 offset:7168
	s_waitcnt lgkmcnt(3)
	v_mfma_f32_16x16x32_bf16 v[88:91], v[136:139], v[156:159], v[52:55]
	ds_read_b128 v[156:159], v115 offset:8192
	s_waitcnt lgkmcnt(3)
	v_mfma_f32_16x16x32_bf16 v[84:87], v[136:139], v[160:163], v[56:59]
	ds_read_b128 v[160:163], v115 offset:9216
	s_waitcnt lgkmcnt(3)
	v_mfma_f32_16x16x32_bf16 v[80:83], v[136:139], v[164:167], v[60:63]
	ds_read_b128 v[164:167], v115 offset:10240
	s_waitcnt lgkmcnt(3)
	v_mfma_f32_16x16x32_bf16 v[76:79], v[136:139], v[132:135], v[64:67]
	ds_read_b128 v[132:135], v115 offset:11264
	s_waitcnt lgkmcnt(3)
	v_mfma_f32_16x16x32_bf16 v[148:151], v[140:143], v[156:159], v[148:151]
	ds_read_b128 v[156:159], v115 offset:12288
	s_waitcnt lgkmcnt(3)
	v_mfma_f32_16x16x32_bf16 v[152:155], v[140:143], v[160:163], v[152:155]
	ds_read_b128 v[160:163], v115 offset:13312
	s_waitcnt lgkmcnt(3)
	v_mfma_f32_16x16x32_bf16 v[96:99], v[140:143], v[164:167], v[96:99]
	ds_read_b128 v[164:167], v115 offset:14336
	s_waitcnt lgkmcnt(3)
	v_mfma_f32_16x16x32_bf16 v[92:95], v[140:143], v[132:135], v[92:95]
	ds_read_b128 v[132:135], v115 offset:15360
	s_waitcnt lgkmcnt(3)
	v_mfma_f32_16x16x32_bf16 v[88:91], v[140:143], v[156:159], v[88:91]
	ds_read_b128 v[156:159], v115 offset:16384
	s_waitcnt lgkmcnt(3)
	v_mfma_f32_16x16x32_bf16 v[84:87], v[140:143], v[160:163], v[84:87]
	ds_read_b128 v[160:163], v115 offset:17408
	s_waitcnt lgkmcnt(3)
	v_mfma_f32_16x16x32_bf16 v[80:83], v[140:143], v[164:167], v[80:83]
	ds_read_b128 v[164:167], v115 offset:18432
	s_waitcnt lgkmcnt(3)
	v_mfma_f32_16x16x32_bf16 v[76:79], v[140:143], v[132:135], v[76:79]
	ds_read_b128 v[132:135], v115 offset:19456
	s_waitcnt lgkmcnt(3)
	s_mov_b32 m0, s47
	s_nop 0
	buffer_load_dwordx4 v113, s[12:15], s61 offen sc0 nt lds
	s_cmp_eq_u32 s63, 0
	s_cbranch_scc1 .Lmain_noburst
	s_or_b32 s62, s61, 0x800
	s_mov_b32 m0, s48
	s_nop 0
	buffer_load_dwordx4 v113, s[12:15], s62 offen sc0 nt lds
	s_or_b32 s62, s61, 0x1000
	s_mov_b32 m0, s49
	s_nop 0
	buffer_load_dwordx4 v113, s[12:15], s62 offen sc0 nt lds
	s_or_b32 s62, s61, 0x1800
	s_mov_b32 m0, s50
	s_nop 0
	buffer_load_dwordx4 v113, s[12:15], s62 offen sc0 nt lds
	s_or_b32 s62, s61, 0x100
	s_mov_b32 m0, s51
	s_nop 0
	buffer_load_dwordx4 v113, s[12:15], s62 offen sc0 nt lds
	s_or_b32 s62, s61, 0x900
	s_mov_b32 m0, s52
	s_nop 0
	buffer_load_dwordx4 v113, s[12:15], s62 offen sc0 nt lds
	s_or_b32 s62, s61, 0x1100
	s_mov_b32 m0, s53
	s_nop 0
	buffer_load_dwordx4 v113, s[12:15], s62 offen sc0 nt lds
	s_or_b32 s62, s61, 0x1900
	s_mov_b32 m0, s54
	s_nop 0
	buffer_load_dwordx4 v113, s[12:15], s62 offen sc0 nt lds
.Lmain_noburst:
	v_mfma_f32_16x16x32_bf16 v[148:151], v[144:147], v[156:159], v[148:151]
	ds_read_b128 v[156:159], v115 offset:20480
	s_waitcnt lgkmcnt(3)
	v_mfma_f32_16x16x32_bf16 v[152:155], v[144:147], v[160:163], v[152:155]
	ds_read_b128 v[160:163], v115 offset:21504
	s_waitcnt lgkmcnt(3)
	v_mfma_f32_16x16x32_bf16 v[96:99], v[144:147], v[164:167], v[96:99]
	ds_read_b128 v[164:167], v115 offset:22528
	s_waitcnt lgkmcnt(3)
	v_mfma_f32_16x16x32_bf16 v[92:95], v[144:147], v[132:135], v[92:95]
	ds_read_b128 v[132:135], v115 offset:23552
	s_waitcnt lgkmcnt(3)
	v_mfma_f32_16x16x32_bf16 v[88:91], v[144:147], v[156:159], v[88:91]
	ds_read_b128 v[156:159], v115 offset:24576
	s_waitcnt lgkmcnt(3)
	v_mfma_f32_16x16x32_bf16 v[84:87], v[144:147], v[160:163], v[84:87]
	ds_read_b128 v[160:163], v115 offset:25600
	s_waitcnt lgkmcnt(3)
	v_mfma_f32_16x16x32_bf16 v[80:83], v[144:147], v[164:167], v[80:83]
	ds_read_b128 v[164:167], v115 offset:26624
	s_waitcnt lgkmcnt(3)
	v_mfma_f32_16x16x32_bf16 v[76:79], v[144:147], v[132:135], v[76:79]
	ds_read_b128 v[132:135], v115 offset:27648
	s_waitcnt lgkmcnt(3)
	v_mfma_f32_16x16x32_bf16 v[148:151], v[128:131], v[156:159], v[148:151]
	ds_read_b128 v[156:159], v115 offset:28672
	s_waitcnt lgkmcnt(3)
	v_mfma_f32_16x16x32_bf16 v[152:155], v[128:131], v[160:163], v[152:155]
	ds_read_b128 v[160:163], v115 offset:29696
	s_waitcnt lgkmcnt(3)
	v_mfma_f32_16x16x32_bf16 v[96:99], v[128:131], v[164:167], v[96:99]
	ds_read_b128 v[164:167], v115 offset:30720
	s_waitcnt lgkmcnt(3)
	v_mfma_f32_16x16x32_bf16 v[92:95], v[128:131], v[132:135], v[92:95]
	ds_read_b128 v[132:135], v115 offset:31744
	s_waitcnt lgkmcnt(3)
	v_mfma_f32_16x16x32_bf16 v[88:91], v[128:131], v[156:159], v[88:91]
	s_waitcnt lgkmcnt(2)
	v_mfma_f32_16x16x32_bf16 v[84:87], v[128:131], v[160:163], v[84:87]
	s_waitcnt lgkmcnt(1)
	v_mfma_f32_16x16x32_bf16 v[80:83], v[128:131], v[164:167], v[80:83]
	s_waitcnt lgkmcnt(0)
	v_mfma_f32_16x16x32_bf16 v[76:79], v[128:131], v[132:135], v[76:79]
	s_cmp_lg_u32 s63, 0
	s_cbranch_scc1 .Lmain_skip1
	s_or_b32 s62, s61, 0x800
	s_mov_b32 m0, s48
	s_nop 0
	buffer_load_dwordx4 v113, s[12:15], s62 offen sc0 nt lds
.Lmain_skip1:
	ds_read2_b32 v[136:137], v114 offset0:128 offset1:144
	ds_read2_b32 v[138:139], v125 offset1:16
	ds_read2_b32 v[140:141], v114 offset0:160 offset1:176
	ds_read2_b32 v[142:143], v125 offset0:32 offset1:48
	ds_read2_b32 v[144:145], v114 offset0:192 offset1:208
	ds_read2_b32 v[146:147], v125 offset0:64 offset1:80
	ds_read2_b32 v[156:157], v114 offset0:224 offset1:240
	ds_read2_b32 v[158:159], v125 offset0:96 offset1:112
	v_fma_f32 v70, v149, v149, 0
	v_fmac_f32_e32 v70, v153, v153
	v_fmac_f32_e32 v70, v97, v97
	v_fmac_f32_e32 v70, v93, v93
	v_fmac_f32_e32 v70, v89, v89
	v_fmac_f32_e32 v70, v85, v85
	v_fmac_f32_e32 v70, v81, v81
	v_fmac_f32_e32 v70, v77, v77
	v_fma_f32 v68, v148, v148, 0
	v_fmac_f32_e32 v68, v152, v152
	v_add_f32_dpp v70, v70, v70 quad_perm:[1,0,3,2] row_mask:0xf bank_mask:0xf bound_ctrl:1
	v_fmac_f32_e32 v68, v96, v96
	v_fmac_f32_e32 v68, v92, v92
	v_add_f32_dpp v70, v70, v70 quad_perm:[2,3,0,1] row_mask:0xf bank_mask:0xf bound_ctrl:1
	v_fmac_f32_e32 v68, v88, v88
	v_fmac_f32_e32 v68, v84, v84
	v_add_f32_dpp v70, v70, v70 row_half_mirror row_mask:0xf bank_mask:0xf bound_ctrl:1
	v_fmac_f32_e32 v68, v80, v80
	v_fmac_f32_e32 v68, v76, v76
	v_add_f32_dpp v70, v70, v70 row_mirror row_mask:0xf bank_mask:0xf bound_ctrl:1
	v_fmamk_f32 v70, v70, 0x3c000000, v124
	s_cmp_lg_u32 s63, 0
	s_cbranch_scc1 .Lmain_skip2
	s_or_b32 s62, s61, 0x1000
	s_mov_b32 m0, s49
	s_nop 0
	buffer_load_dwordx4 v113, s[12:15], s62 offen sc0 nt lds
.Lmain_skip2:
	v_rsq_f32_e32 v127, v70
	v_fma_f32 v70, v150, v150, 0
	v_fmac_f32_e32 v70, v154, v154
	v_fmac_f32_e32 v70, v98, v98
	v_fmac_f32_e32 v70, v94, v94
	v_fmac_f32_e32 v70, v90, v90
	v_fmac_f32_e32 v70, v86, v86
	v_fmac_f32_e32 v70, v82, v82
	v_fmac_f32_e32 v70, v78, v78
	v_add_f32_dpp v68, v68, v68 quad_perm:[1,0,3,2] row_mask:0xf bank_mask:0xf bound_ctrl:1
	v_mul_f32_e32 v131, v127, v149
	v_add_f32_dpp v70, v70, v70 quad_perm:[1,0,3,2] row_mask:0xf bank_mask:0xf bound_ctrl:1
	v_add_f32_dpp v68, v68, v68 quad_perm:[2,3,0,1] row_mask:0xf bank_mask:0xf bound_ctrl:1
	v_mul_f32_e32 v81, v127, v81
	v_add_f32_dpp v70, v70, v70 quad_perm:[2,3,0,1] row_mask:0xf bank_mask:0xf bound_ctrl:1
	v_add_f32_dpp v68, v68, v68 row_half_mirror row_mask:0xf bank_mask:0xf bound_ctrl:1
	v_cmp_gt_u32_e64 s[0:1], s55, v72
	v_add_f32_dpp v70, v70, v70 row_half_mirror row_mask:0xf bank_mask:0xf bound_ctrl:1
	v_add_f32_dpp v68, v68, v68 row_mirror row_mask:0xf bank_mask:0xf bound_ctrl:1
	v_fmamk_f32 v68, v68, 0x3c000000, v124
	v_add_f32_dpp v70, v70, v70 row_mirror row_mask:0xf bank_mask:0xf bound_ctrl:1
	v_fmamk_f32 v70, v70, 0x3c000000, v124
	v_rsq_f32_e32 v130, v70
	v_fma_f32 v70, v151, v151, 0
	v_fmac_f32_e32 v70, v155, v155
	v_fmac_f32_e32 v70, v99, v99
	v_fmac_f32_e32 v70, v95, v95
	v_fmac_f32_e32 v70, v91, v91
	v_fmac_f32_e32 v70, v87, v87
	v_fmac_f32_e32 v70, v83, v83
	v_fmac_f32_e32 v70, v79, v79
	v_rsq_f32_e32 v68, v68
	v_mul_f32_e32 v98, v130, v98
	v_add_f32_dpp v70, v70, v70 quad_perm:[1,0,3,2] row_mask:0xf bank_mask:0xf bound_ctrl:1
	v_mul_f32_e32 v90, v130, v90
	v_mul_f32_e32 v111, v68, v148
	v_add_f32_dpp v110, v70, v70 quad_perm:[2,3,0,1] row_mask:0xf bank_mask:0xf bound_ctrl:1
	s_nop 1
	v_add_f32_dpp v110, v110, v110 row_half_mirror row_mask:0xf bank_mask:0xf bound_ctrl:1
	v_mul_f32_e32 v96, v68, v96
	v_mul_f32_e32 v92, v68, v92
	v_add_f32_dpp v110, v110, v110 row_mirror row_mask:0xf bank_mask:0xf bound_ctrl:1
	v_fmamk_f32 v110, v110, 0x3c000000, v124
	s_waitcnt lgkmcnt(0)
	s_cmp_lg_u32 s63, 0
	s_cbranch_scc1 .Lmain_skip3
	s_or_b32 s62, s61, 0x1800
	s_mov_b32 m0, s50
	s_nop 0
	buffer_load_dwordx4 v113, s[12:15], s62 offen sc0 nt lds
.Lmain_skip3:
	v_fma_f32 v111, v111, v136, v138
	v_fma_f32 v131, v131, v136, v138
	v_exp_f32_e32 v111, v111
	v_exp_f32_e32 v131, v131
	v_rsq_f32_e32 v132, v110
	v_mul_f32_e32 v88, v68, v88
	v_add_f32_e32 v110, 1.0, v111
	v_add_f32_e32 v111, 1.0, v131
	v_mul_f32_e32 v131, v130, v150
	v_mul_f32_e32 v133, v132, v151
	v_fma_f32 v131, v131, v136, v138
	v_fma_f32 v70, v133, v136, v138
	v_exp_f32_e32 v131, v131
	v_exp_f32_e32 v70, v70
	v_rcp_f32_e32 v110, v110
	v_rcp_f32_e32 v111, v111
	v_add_f32_e32 v128, 1.0, v131
	v_add_f32_e32 v70, 1.0, v70
	v_rcp_f32_e32 v128, v128
	v_rcp_f32_e32 v70, v70
	v_mul_f32_e32 v131, v68, v152
	v_fma_f32 v131, v131, v137, v139
	v_cvt_pk_bf16_f32 v110, v110, v111
	v_cvt_pk_bf16_f32 v111, v128, v70
	v_mul_f32_e32 v128, v127, v153
	v_exp_f32_e32 v131, v131
	v_fma_f32 v128, v128, v137, v139
	v_exp_f32_e32 v128, v128
	v_mul_f32_e32 v99, v132, v99
	v_add_f32_e32 v70, 1.0, v131
	v_rcp_f32_e32 v133, v70
	v_add_f32_e32 v70, 1.0, v128
	v_mul_f32_e32 v131, v130, v154
	v_rcp_f32_e32 v134, v70
	v_mul_f32_e32 v70, v132, v155
	v_fma_f32 v131, v131, v137, v139
	v_fma_f32 v129, v70, v137, v139
	v_exp_f32_e32 v135, v129
	v_exp_f32_e32 v131, v131
	v_mul_f32_e32 v91, v132, v91
	v_add_f32_e32 v135, 1.0, v135
	v_rcp_f32_e32 v135, v135
	s_cmp_lg_u32 s63, 0
	s_cbranch_scc1 .Lmain_skip4
	s_or_b32 s62, s61, 0x100
	s_mov_b32 m0, s51
	s_nop 0
	buffer_load_dwordx4 v113, s[12:15], s62 offen sc0 nt lds
.Lmain_skip4:
	v_fma_f32 v96, v96, v140, v142
	v_exp_f32_e32 v136, v96
	v_mul_f32_e32 v96, v127, v97
	v_fma_f32 v96, v96, v140, v142
	v_exp_f32_e32 v97, v96
	v_fma_f32 v98, v98, v140, v142
	v_fma_f32 v70, v99, v140, v142
	v_exp_f32_e32 v98, v98
	v_exp_f32_e32 v70, v70
	v_add_f32_e32 v97, 1.0, v97
	v_cvt_pk_bf16_f32 v96, v133, v134
	v_add_f32_e32 v133, 1.0, v136
	v_rcp_f32_e32 v99, v97
	v_add_f32_e32 v97, 1.0, v98
	v_add_f32_e32 v70, 1.0, v70
	v_fma_f32 v92, v92, v141, v143
	v_rcp_f32_e32 v133, v133
	v_rcp_f32_e32 v128, v97
	v_rcp_f32_e32 v70, v70
	v_exp_f32_e32 v92, v92
	v_cvt_pk_bf16_f32 v98, v133, v99
	v_add_f32_e32 v131, 1.0, v131
	v_cvt_pk_bf16_f32 v99, v128, v70
	v_add_f32_e32 v70, 1.0, v92
	v_mul_f32_e32 v92, v127, v93
	v_fma_f32 v92, v92, v141, v143
	v_exp_f32_e32 v92, v92
	v_mul_f32_e32 v93, v130, v94
	v_fma_f32 v93, v93, v141, v143
	v_rcp_f32_e32 v131, v131
	v_exp_f32_e32 v93, v93
	v_rcp_f32_e32 v94, v70
	v_add_f32_e32 v70, 1.0, v92
	v_rcp_f32_e32 v128, v70
	v_mul_f32_e32 v70, v132, v95
	v_cvt_pk_bf16_f32 v97, v131, v135
	v_add_f32_e32 v131, 1.0, v93
	v_fma_f32 v129, v70, v141, v143
	v_exp_f32_e32 v95, v129
	v_rcp_f32_e32 v129, v131
	v_mul_f32_e32 v84, v68, v84
	v_mul_f32_e32 v80, v68, v80
	s_cmp_lg_u32 s63, 0
	s_cbranch_scc1 .Lmain_skip5
	s_or_b32 s62, s61, 0x900
	s_mov_b32 m0, s52
	s_nop 0
	buffer_load_dwordx4 v113, s[12:15], s62 offen sc0 nt lds
.Lmain_skip5:
	v_fma_f32 v88, v88, v144, v146
	v_exp_f32_e32 v131, v88
	v_mul_f32_e32 v88, v127, v89
	v_fma_f32 v88, v88, v144, v146
	v_exp_f32_e32 v89, v88
	v_fma_f32 v90, v90, v144, v146
	v_fma_f32 v70, v91, v144, v146
	v_exp_f32_e32 v90, v90
	v_exp_f32_e32 v70, v70
	v_add_f32_e32 v89, 1.0, v89
	v_cvt_pk_bf16_f32 v88, v94, v128
	v_add_f32_e32 v94, 1.0, v131
	v_rcp_f32_e32 v91, v89
	v_add_f32_e32 v89, 1.0, v90
	v_add_f32_e32 v70, 1.0, v70
	v_fma_f32 v84, v84, v145, v147
	v_rcp_f32_e32 v94, v94
	v_rcp_f32_e32 v92, v89
	v_rcp_f32_e32 v70, v70
	v_exp_f32_e32 v84, v84
	v_cvt_pk_bf16_f32 v90, v94, v91
	v_mul_f32_e32 v68, v68, v76
	v_cvt_pk_bf16_f32 v91, v92, v70
	v_add_f32_e32 v70, 1.0, v84
	v_mul_f32_e32 v84, v127, v85
	v_fma_f32 v84, v84, v145, v147
	v_mul_f32_e32 v85, v130, v86
	v_exp_f32_e32 v84, v84
	v_fma_f32 v85, v85, v145, v147
	v_exp_f32_e32 v85, v85
	v_rcp_f32_e32 v92, v70
	v_add_f32_e32 v70, 1.0, v84
	v_rcp_f32_e32 v84, v70
	v_add_f32_e32 v70, 1.0, v85
	v_mul_f32_e32 v85, v132, v87
	v_fma_f32 v93, v85, v145, v147
	v_exp_f32_e32 v85, v93
	v_rcp_f32_e32 v93, v70
	v_mul_f32_e32 v76, v127, v77
	v_mul_f32_e32 v82, v130, v82
	v_mul_f32_e32 v83, v132, v83
	v_mul_f32_e32 v77, v130, v78
	s_cmp_lg_u32 s63, 0
	s_cbranch_scc1 .Lmain_skip6
	s_or_b32 s62, s61, 0x1100
	s_mov_b32 m0, s53
	s_nop 0
	buffer_load_dwordx4 v113, s[12:15], s62 offen sc0 nt lds
.Lmain_skip6:
	v_fma_f32 v76, v76, v157, v159
	v_mul_f32_e32 v78, v132, v79
	v_fma_f32 v80, v80, v156, v158
	v_fma_f32 v81, v81, v156, v158
	v_fma_f32 v82, v82, v156, v158
	v_fma_f32 v70, v83, v156, v158
	v_fma_f32 v68, v68, v157, v159
	v_exp_f32_e32 v76, v76
	v_fma_f32 v77, v77, v157, v159
	v_fma_f32 v87, v78, v157, v159
	v_exp_f32_e32 v82, v82
	v_exp_f32_e32 v70, v70
	v_exp_f32_e32 v68, v68
	v_exp_f32_e32 v77, v77
	v_exp_f32_e32 v71, v87
	v_add_f32_e32 v76, 1.0, v76
	v_add_f32_e32 v82, 1.0, v82
	v_add_f32_e32 v70, 1.0, v70
	v_add_f32_e32 v68, 1.0, v68
	v_rcp_f32_e32 v78, v76
	v_add_f32_e32 v76, 1.0, v77
	v_add_f32_e32 v71, 1.0, v71
	v_rcp_f32_e32 v82, v82
	v_rcp_f32_e32 v70, v70
	v_rcp_f32_e32 v68, v68
	v_rcp_f32_e32 v79, v76
	v_rcp_f32_e32 v71, v71
	v_exp_f32_e32 v80, v80
	v_exp_f32_e32 v81, v81
	v_cvt_pk_bf16_f32 v77, v82, v70
	v_cvt_pk_bf16_f32 v78, v68, v78
	v_cvt_pk_bf16_f32 v79, v79, v71
	v_subrev_u32_e32 v68, s16, v72
	v_subrev_u32_e32 v70, s16, v73
	v_subrev_u32_e32 v71, s16, v74
	v_add_f32_e32 v95, 1.0, v95
	v_add_f32_e32 v85, 1.0, v85
	v_add_f32_e32 v80, 1.0, v80
	v_add_f32_e32 v81, 1.0, v81
	s_cmp_lg_u32 s63, 0
	s_cbranch_scc1 .Lmain_skip7
	s_or_b32 s62, s61, 0x1900
	s_mov_b32 m0, s54
	s_nop 0
	buffer_load_dwordx4 v113, s[12:15], s62 offen sc0 nt lds
